# queue: next item index fetched by thread 0 at the start of the attention epilogue (late pop prefetch) + kn2 hoist + rank flatten on v73
# speedup vs baseline: 1.0155x; 1.0124x over previous
.LBB0_407:
	s_add_u32 s0, s36, s6
	s_addc_u32 s1, s37, s7
	global_load_dwordx4 v[4:7], v1, s[0:1]
	global_load_dwordx4 v[8:11], v1, s[0:1] offset:16
	s_add_u32 s0, s38, s6
	s_addc_u32 s1, s39, s7
	global_load_dwordx4 v[12:15], v1, s[0:1]
	global_load_dwordx4 v[16:19], v1, s[0:1] offset:16
	s_add_u32 s0, s40, s6
	s_addc_u32 s1, s41, s7
	global_load_dwordx4 v[20:23], v1, s[0:1]
	global_load_dwordx4 v[24:27], v1, s[0:1] offset:16
	s_add_u32 s0, s42, s6
	s_addc_u32 s1, s43, s7
	global_load_dwordx4 v[28:31], v1, s[0:1]
	global_load_dwordx4 v[32:35], v1, s[0:1] offset:16
	s_add_u32 s6, s6, 32
	s_addc_u32 s7, s7, 0
	s_cmpk_eq_i32 s6, 0x100
	s_waitcnt vmcnt(7)
	v_mov_b32_e32 v36, v4
	v_mov_b32_e32 v4, v6
	s_waitcnt vmcnt(6)
	v_mov_b32_e32 v6, v8
	v_mov_b32_e32 v8, v10
	s_waitcnt vmcnt(5)
	v_mov_b32_e32 v10, v12
	v_mov_b32_e32 v12, v14
	s_waitcnt vmcnt(3)
	v_mov_b32_e32 v37, v20
	v_mov_b32_e32 v20, v5
	v_mov_b32_e32 v5, v22
	v_mov_b32_e32 v22, v7
	s_waitcnt vmcnt(2)
	v_mov_b32_e32 v7, v24
	v_mov_b32_e32 v24, v9
	v_mov_b32_e32 v9, v26
	v_mov_b32_e32 v26, v11
	s_waitcnt vmcnt(1)
	v_mov_b32_e32 v11, v28
	v_mov_b32_e32 v28, v13
	v_pk_fma_f32 v[2:3], v[36:37], v[10:11], v[2:3]
	v_mov_b32_e32 v13, v30
	v_pk_fma_f32 v[2:3], v[20:21], v[28:29], v[2:3]
	v_mov_b32_e32 v30, v15
	v_pk_fma_f32 v[2:3], v[4:5], v[12:13], v[2:3]
	v_mov_b32_e32 v14, v16
	s_waitcnt vmcnt(0)
	v_mov_b32_e32 v15, v32
	v_pk_fma_f32 v[2:3], v[22:23], v[30:31], v[2:3]
	v_mov_b32_e32 v32, v17
	v_pk_fma_f32 v[2:3], v[6:7], v[14:15], v[2:3]
	v_mov_b32_e32 v16, v18
	v_mov_b32_e32 v17, v34
	v_pk_fma_f32 v[2:3], v[24:25], v[32:33], v[2:3]
	v_mov_b32_e32 v34, v19
	v_pk_fma_f32 v[2:3], v[8:9], v[16:17], v[2:3]
	s_nop 0
	v_pk_fma_f32 v[2:3], v[26:27], v[34:35], v[2:3]
	s_cbranch_scc0 .LBB0_407
	v_mul_f32_e32 v1, 0x3fb8aa3b, v2
	v_mul_f32_e32 v2, 0x3fb8aa3b, v3
	v_exp_f32_e32 v1, v1
	v_exp_f32_e32 v2, v2
	s_add_u32 s0, s22, 0x4000000
	s_addc_u32 s1, s23, 0
	v_writelane_b32 v255, s0, 17
	v_sub_f32_e32 v1, v1, v2
	s_add_u32 s64, s20, 0x8000000
	v_add_f32_e32 v198, 0x3e4ccccd, v1
	v_writelane_b32 v255, s1, 18
	s_addc_u32 s65, s21, 0
	s_add_i32 s55, 0, 0x19000
	s_add_i32 s0, 0, 0x18c10
	s_mov_b32 s42, -2.0
	s_mov_b32 s48, 0xc1000000
	s_mov_b32 s50, 0xc1200000
	s_mov_b32 s56, 0xc1800000
	s_mov_b32 s58, 0xc1900000
	s_mov_b32 s60, 0xc1c00000
	s_mov_b32 s62, 0xc1d00000
	s_mov_b32 s68, 0xc2200000
	s_mov_b32 s70, 0xc2280000
	s_mov_b32 s72, 0xc2400000
	s_mov_b32 s74, 0xc2480000
	s_mov_b32 s76, 0xc2600000
	s_mov_b32 s78, 0xc2680000
	v_mov_b32_e32 v199, v198
	s_mov_b32 s41, 0
	s_mov_b64 s[6:7], -1
	v_mov_b32_e32 v3, 0
	s_movk_i32 s33, 0x2000
	s_movk_i32 s52, 0x4000
	s_movk_i32 s53, 0x6000
	s_mov_b32 s37, 0x8000
	s_mov_b32 s66, 0xa000
	s_mov_b32 s67, 0xc000
	s_mov_b32 s83, 0xe000
	s_mov_b32 s90, 0x10000
	s_mov_b32 s91, 0x12000
	s_mov_b32 s92, 0x14000
	s_mov_b32 s93, 0x16000
	s_movk_i32 s80, 0x1000
	s_movk_i32 s81, 0x3000
	s_movk_i32 s28, 0x5000
	s_mov_b32 s29, 0x40000
	s_mov_b32 s30, 0x41000
	v_writelane_b32 v255, s0, 19
	v_mov_b32_e32 v1, 0x260
	v_mov_b32_e32 v201, 2.0
	s_mov_b32 s43, 0xc0400000
	s_mov_b32 s49, 0xc1100000
	s_mov_b32 s51, 0xc1300000
	s_mov_b32 s57, 0xc1880000
	s_mov_b32 s59, 0xc1980000
	s_mov_b32 s61, 0xc1c80000
	s_mov_b32 s63, 0xc1d80000
	s_mov_b32 s69, 0xc2240000
	s_mov_b32 s71, 0xc22c0000
	s_mov_b32 s73, 0xc2440000
	s_mov_b32 s75, 0xc24c0000
	s_mov_b32 s77, 0xc2640000
	s_mov_b32 s79, 0xc26c0000
	s_mov_b32 s36, 0x41000000
	s_movk_i32 s4, 0x7fff
	v_mov_b32_e32 v213, s55
	v_mov_b32_e32 v214, 0x42800000
	v_mbcnt_hi_u32_b32 v212, -1, v196
	v_mov_b32_e32 v215, 0xf149f2ca
	s_mov_b64 s[84:85], -1
	s_mov_b32 s5, 0
	s_mov_b32 s32, 0
	s_branch .LBB0_412

.LBB0_412:
	s_bitcmp0_b32 s5, 0
	s_cselect_b64 s[0:1], -1, 0
	s_xor_b64 s[8:9], s[84:85], -1
	s_or_b64 s[0:1], s[8:9], s[0:1]
	s_and_b64 s[8:9], s[6:7], s[0:1]
	s_barrier
	s_and_saveexec_b64 s[10:11], s[94:95]
	s_cbranch_execz .LBB0_416
	s_mov_b64 s[88:89], exec
	v_mbcnt_lo_u32_b32 v2, s88, 0
	v_mbcnt_hi_u32_b32 v2, s89, v2
	v_cmp_eq_u32_e32 vcc, 0, v2
	s_and_saveexec_b64 s[86:87], vcc
	s_cbranch_execz .LBB0_415
	s_and_b64 s[0:1], s[8:9], exec
	s_cselect_b32 s31, 1, 2
	s_cmp_eq_u32 s31, s32
	s_mov_b32 s32, 0
	s_cbranch_scc0 .Lmy_pop_atomic
	s_waitcnt vmcnt(0)
	v_mov_b32_e32 v4, v254
	s_branch .LBB0_415
.Lmy_pop_atomic:
	s_and_b64 s[0:1], s[8:9], exec
	s_cselect_b32 s0, 0, 16
	v_readlane_b32 s34, v255, 15
	v_readlane_b32 s35, v255, 16
	s_add_u32 s0, s34, s0
	s_addc_u32 s1, s35, 0
	s_bcnt1_i32_b64 s31, s[88:89]
	v_mov_b32_e32 v4, s31
	global_atomic_add v4, v3, v4, s[0:1] offset:32 sc0

.LBB0_553:
	s_bitcmp1_b32 s5, 0
	s_cselect_b64 s[6:7], -1, 0
	s_orn2_b64 s[6:7], s[6:7], s[84:85]
	s_cmp_lg_u64 s[6:7], 0
	s_cselect_b32 s31, 32, 48
	s_cselect_b32 s32, 1, 2
	v_readlane_b32 s6, v255, 15
	v_readlane_b32 s7, v255, 16
	v_mov_b32_e32 v253, 1
	v_cmp_eq_u32_e64 s[8:9], 0, v0
	s_add_u32 s6, s6, s31
	s_addc_u32 s7, s7, 0
	s_and_saveexec_b64 s[34:35], s[8:9]
	s_cbranch_execz .Lmy_pf_skip
	global_atomic_add v254, v3, v253, s[6:7] sc0
.Lmy_pf_skip:
	s_or_b64 exec, exec, s[34:35]
	s_mov_b32 s92, 0x14000
	s_mov_b32 s93, 0x16000
	s_mov_b64 s[64:65], s[66:67]
	v_cmp_gt_f32_e32 vcc, 1.0, v98
	s_mov_b32 s55, s37
	s_mov_b32 s66, 0xa000
	s_mov_b32 s67, 0xc000
	s_cbranch_vccz .LBB0_558
	v_cmp_gt_u32_e32 vcc, 32, v223
	s_and_saveexec_b64 s[6:7], vcc
	s_mov_b32 s37, 0x8000
	ds_write_b32 v230, v98 offset:128
	s_or_b64 exec, exec, s[6:7]
	s_waitcnt lgkmcnt(0)
	ds_read_b128 v[4:7], v229 offset:224
	ds_read_b128 v[8:11], v229 offset:192
	ds_read_b128 v[12:15], v229 offset:160
	ds_read_b128 v[16:19], v229 offset:128
	s_waitcnt lgkmcnt(0)
	v_pk_mul_f32 v[96:97], v[96:97], v[6:7]
	v_pk_mul_f32 v[92:93], v[92:93], v[10:11]
	v_pk_mul_f32 v[88:89], v[88:89], v[14:15]
	v_pk_mul_f32 v[84:85], v[84:85], v[18:19]
	v_pk_mul_f32 v[94:95], v[94:95], v[4:5]
	v_pk_mul_f32 v[90:91], v[90:91], v[8:9]
	v_pk_mul_f32 v[86:87], v[86:87], v[12:13]
	v_pk_mul_f32 v[82:83], v[82:83], v[16:17]
	v_pk_mul_f32 v[80:81], v[80:81], v[6:7]
	v_pk_mul_f32 v[76:77], v[76:77], v[10:11]
	v_pk_mul_f32 v[72:73], v[72:73], v[14:15]
	v_pk_mul_f32 v[68:69], v[68:69], v[18:19]
	v_pk_mul_f32 v[78:79], v[78:79], v[4:5]
	v_pk_mul_f32 v[74:75], v[74:75], v[8:9]
	v_pk_mul_f32 v[70:71], v[70:71], v[12:13]
	v_pk_mul_f32 v[66:67], v[66:67], v[16:17]
	v_pk_mul_f32 v[64:65], v[64:65], v[6:7]
	v_pk_mul_f32 v[60:61], v[60:61], v[10:11]
	v_pk_mul_f32 v[56:57], v[56:57], v[14:15]
	v_pk_mul_f32 v[52:53], v[52:53], v[18:19]
	v_pk_mul_f32 v[62:63], v[62:63], v[4:5]
	v_pk_mul_f32 v[58:59], v[58:59], v[8:9]
	v_pk_mul_f32 v[54:55], v[54:55], v[12:13]
	v_pk_mul_f32 v[50:51], v[50:51], v[16:17]
	v_pk_mul_f32 v[48:49], v[48:49], v[6:7]
	v_pk_mul_f32 v[44:45], v[44:45], v[10:11]
	v_pk_mul_f32 v[40:41], v[40:41], v[14:15]
	v_pk_mul_f32 v[36:37], v[36:37], v[18:19]
	v_pk_mul_f32 v[46:47], v[46:47], v[4:5]
	v_pk_mul_f32 v[42:43], v[42:43], v[8:9]
	v_pk_mul_f32 v[38:39], v[38:39], v[12:13]
	v_pk_mul_f32 v[34:35], v[34:35], v[16:17]
	s_branch .LBB0_559
